# prep partition blocks: sorted-chunk copy-out issues its 13 LDS reads before the stores
# speedup vs baseline: 1.0184x; 1.0017x over previous
.LBB0_134:
	ds_read_b32 v13, v12
	ds_read_b32 v14, v12 offset:1024
	ds_read_b32 v15, v12 offset:2048
	ds_read_b32 v16, v12 offset:3072
	ds_read_b32 v17, v12 offset:4096
	ds_read_b32 v18, v12 offset:5120
	ds_read_b32 v19, v12 offset:6144
	ds_read_b32 v20, v12 offset:7168
	ds_read_b32 v21, v12 offset:8192
	ds_read_b32 v22, v12 offset:9216
	ds_read_b32 v23, v12 offset:10240
	ds_read_b32 v24, v12 offset:11264
	ds_read_b32 v25, v12 offset:12288
	s_movk_i32 s0, 0x1000
	v_add_co_u32_e32 v26, vcc, s0, v0
	s_nop 1
	v_addc_co_u32_e32 v27, vcc, 0, v1, vcc
	s_movk_i32 s0, 0x2000
	v_add_co_u32_e32 v28, vcc, s0, v0
	s_nop 1
	v_addc_co_u32_e32 v29, vcc, 0, v1, vcc
	s_movk_i32 s0, 0x3000
	v_add_co_u32_e32 v30, vcc, s0, v0
	s_nop 1
	v_addc_co_u32_e32 v31, vcc, 0, v1, vcc
	s_waitcnt lgkmcnt(0)
	global_store_dword v[0:1], v13, off
	global_store_dword v[0:1], v14, off offset:1024
	global_store_dword v[0:1], v15, off offset:2048
	global_store_dword v[0:1], v16, off offset:3072
	global_store_dword v[26:27], v17, off
	global_store_dword v[26:27], v18, off offset:1024
	global_store_dword v[26:27], v19, off offset:2048
	global_store_dword v[26:27], v20, off offset:3072
	global_store_dword v[28:29], v21, off
	global_store_dword v[28:29], v22, off offset:1024
	global_store_dword v[28:29], v23, off offset:2048
	global_store_dword v[28:29], v24, off offset:3072
	v_cmp_gt_i32_e32 vcc, 0xffffff35, v2
	s_and_saveexec_b64 s[0:1], vcc
	global_store_dword v[30:31], v25, off
